# register-staged deep-prefetch loader (4 chunks in flight) + 2-slot ring
# speedup vs baseline: 1.0016x; 1.0016x over previous
; DI void gdn_scan_seq(const Params& p, int bh16, char* ldsf) {
;     ...
;   f32x16 S[4];
; #pragma unroll
;   for (int m = 0; m < 4; ++m)
; #pragma unroll
;     for (int r = 0; r < 16; ++r) S[m][r] = 0.f;
;   asm volatile("s_waitcnt vmcnt(0)" ::: "memory");
;   __syncthreads();
;   SCAN_ISSUE(0, 0); SCAN_ISSUE(1, 1);
; DI void phase_mixer(const Params& p, int bid, int nb, char* lds, char* ctl, char* ldsf) {
;     ...
;   if (bid < 32) { if (vb == 0) gdn_scan_seq(p, bid >> 1, ldsf); else { __syncthreads(); for (int k = 0; k < 128; ++k) { __builtin_amdgcn_s_barrier(); asm volatile("" ::: "memory"); } __syncthreads(); } }
.LBB0_1207:
	s_or_b64 exec, exec, s[0:1]
	v_mov_b32_e32 v135, v206
	s_waitcnt lgkmcnt(0)
	s_barrier
	s_and_saveexec_b64 s[0:1], s[6:7]
	s_cbranch_execz .LBB0_1227
	s_movk_i32 s2, 0xff
	v_cmp_lt_u32_e32 vcc, s2, v207
	s_and_saveexec_b64 s[2:3], vcc
	s_xor_b64 s[6:7], exec, s[2:3]
	s_cbranch_execz .LBB0_1212
	v_readlane_b32 s2, v250, 0
	v_lshrrev_b32_e32 v209, 6, v206
	v_and_b32_e32 v208, 63, v206
	v_lshlrev_b32_e32 v132, 12, v209
	v_lshl_or_b32 v132, v208, 4, v132
	v_lshlrev_b32_e32 v133, 11, v209
	v_lshl_or_b32 v133, v208, 5, v133
	v_add_u32_e32 v134, 0x2000, v133
	v_mov_b32_e32 v208, v132
	s_nop 3
	s_lshl_b32 s2, s2, 21
	s_add_u32 s8, s84, s2
	s_addc_u32 s9, s85, 0
	s_add_u32 s12, s8, 0x1c000000
	s_addc_u32 s13, s9, 0
	s_add_u32 s8, s8, 0x1e000000
	s_addc_u32 s9, s9, 0
	s_add_u32 s10, s66, s2
	s_addc_u32 s11, s67, 0
	s_add_u32 s10, s10, 0x2000000
	s_addc_u32 s11, s11, 0
	s_mov_b32 s15, 0
	global_load_dwordx4 v[0:3], v132, s[8:9]
	global_load_dwordx4 v[4:7], v132, s[8:9] offset:1024
	global_load_dwordx4 v[8:11], v132, s[8:9] offset:2048
	global_load_dwordx4 v[12:15], v132, s[8:9] offset:3072
	global_load_dwordx4 v[16:19], v132, s[10:11]
	global_load_dwordx4 v[20:23], v132, s[10:11] offset:1024
	global_load_dwordx4 v[24:27], v132, s[10:11] offset:2048
	global_load_dwordx4 v[28:31], v132, s[10:11] offset:3072
	global_load_dwordx4 v[32:35], v133, s[12:13]
	global_load_dwordx4 v[36:39], v133, s[12:13] offset:16
	global_load_dwordx4 v[40:43], v134, s[12:13]
	global_load_dwordx4 v[44:47], v134, s[12:13] offset:16
	s_add_u32 s15, s15, 1
	s_cmp_lt_u32 s15, 0x80
	s_cselect_b32 s14, 0x4000, 0
	s_add_u32 s8, s8, s14
	s_addc_u32 s9, s9, 0
	s_add_u32 s10, s10, s14
	s_addc_u32 s11, s11, 0
	s_add_u32 s12, s12, s14
	s_addc_u32 s13, s13, 0
	global_load_dwordx4 v[48:51], v132, s[8:9]
	global_load_dwordx4 v[52:55], v132, s[8:9] offset:1024
	global_load_dwordx4 v[56:59], v132, s[8:9] offset:2048
	global_load_dwordx4 v[60:63], v132, s[8:9] offset:3072
	global_load_dwordx4 v[64:67], v132, s[10:11]
	global_load_dwordx4 v[68:71], v132, s[10:11] offset:1024
	global_load_dwordx4 v[72:75], v132, s[10:11] offset:2048
	global_load_dwordx4 v[76:79], v132, s[10:11] offset:3072
	global_load_dwordx4 v[80:83], v133, s[12:13]
	global_load_dwordx4 v[84:87], v133, s[12:13] offset:16
	global_load_dwordx4 v[88:91], v134, s[12:13]
	global_load_dwordx4 v[92:95], v134, s[12:13] offset:16
	s_add_u32 s15, s15, 1
	s_cmp_lt_u32 s15, 0x80
	s_cselect_b32 s14, 0x4000, 0
	s_add_u32 s8, s8, s14
	s_addc_u32 s9, s9, 0
	s_add_u32 s10, s10, s14
	s_addc_u32 s11, s11, 0
	s_add_u32 s12, s12, s14
	s_addc_u32 s13, s13, 0
	global_load_dwordx4 v[96:99], v132, s[8:9]
	global_load_dwordx4 v[100:103], v132, s[8:9] offset:1024
	global_load_dwordx4 v[104:107], v132, s[8:9] offset:2048
	global_load_dwordx4 v[108:111], v132, s[8:9] offset:3072
	global_load_dwordx4 v[112:115], v132, s[10:11]
	global_load_dwordx4 v[116:119], v132, s[10:11] offset:1024
	global_load_dwordx4 v[120:123], v132, s[10:11] offset:2048
	global_load_dwordx4 v[124:127], v132, s[10:11] offset:3072
	global_load_dwordx4 v[128:131], v133, s[12:13]
	global_load_dwordx4 v[136:139], v133, s[12:13] offset:16
	global_load_dwordx4 v[140:143], v134, s[12:13]
	global_load_dwordx4 v[148:151], v134, s[12:13] offset:16
	s_add_u32 s15, s15, 1
	s_cmp_lt_u32 s15, 0x80
	s_cselect_b32 s14, 0x4000, 0
	s_add_u32 s8, s8, s14
	s_addc_u32 s9, s9, 0
	s_add_u32 s10, s10, s14
	s_addc_u32 s11, s11, 0
	s_add_u32 s12, s12, s14
	s_addc_u32 s13, s13, 0
	global_load_dwordx4 v[152:155], v132, s[8:9]
	global_load_dwordx4 v[156:159], v132, s[8:9] offset:1024
	global_load_dwordx4 v[160:163], v132, s[8:9] offset:2048
	global_load_dwordx4 v[164:167], v132, s[8:9] offset:3072
	global_load_dwordx4 v[168:171], v132, s[10:11]
	global_load_dwordx4 v[172:175], v132, s[10:11] offset:1024
	global_load_dwordx4 v[178:181], v132, s[10:11] offset:2048
	global_load_dwordx4 v[182:185], v132, s[10:11] offset:3072
	global_load_dwordx4 v[190:193], v133, s[12:13]
	global_load_dwordx4 v[194:197], v133, s[12:13] offset:16
	global_load_dwordx4 v[198:201], v134, s[12:13]
	global_load_dwordx4 v[202:205], v134, s[12:13] offset:16
	s_add_u32 s15, s15, 1
	s_cmp_lt_u32 s15, 0x80
	s_cselect_b32 s14, 0x4000, 0
	s_add_u32 s8, s8, s14
	s_addc_u32 s9, s9, 0
	s_add_u32 s10, s10, s14
	s_addc_u32 s11, s11, 0
	s_add_u32 s12, s12, s14
	s_addc_u32 s13, s13, 0
	s_mov_b32 s2, 0
	s_mov_b32 s3, 0
	s_barrier
; DI bf16x8 packS(const f32x16& x, int s) { return pack8(x[8 * s], x[8 * s + 1], x[8 * s + 2], x[8 * s + 3], x[8 * s + 4], x[8 * s + 5], x[8 * s + 6], x[8 * s + 7]); }
; DI void gdn_scan_seq(const Params& p, int bh16, char* ldsf) {
;     ...
;   for (int c = 0; c < 128; ++c) {
;     if (c + 1 < 128) asm volatile("s_waitcnt vmcnt(12)" ::: "memory"); else asm volatile("s_waitcnt vmcnt(0)" ::: "memory");
;     __builtin_amdgcn_s_barrier();
;     asm volatile("" ::: "memory");
;     char* sco = scp + (size_t)c * 32768;
;     bf16x8 Sb[4][2];
; #pragma unroll
;     for (int m = 0; m < 4; ++m) { Sb[m][0] = packS(S[m], 0); Sb[m][1] = packS(S[m], 1); *(bf16x8*)(sco + (m * 2 + 0) * 1024) = Sb[m][0]; *(bf16x8*)(sco + (m * 2 + 1) * 1024) = Sb[m][1]; }
;     __builtin_amdgcn_sched_barrier(0);
;     if (c + 2 < 128) { const int s2 = sl >= 1 ? sl - 1 : 2; SCAN_ISSUE(c + 2, s2); }
; DI void phase_mixer(const Params& p, int bid, int nb, char* lds, char* ctl, char* ldsf) {
;     ...
;   if (bid < 32) { if (vb == 0) gdn_scan_seq(p, bid >> 1, ldsf); else { __syncthreads(); for (int k = 0; k < 128; ++k) { __builtin_amdgcn_s_barrier(); asm volatile("" ::: "memory"); } __syncthreads(); } }
.Lshadow_loop:
	s_waitcnt vmcnt(36)
	v_add_u32_e32 v209, s3, v208
	ds_write_b128 v209, v[0:3]
	ds_write_b128 v209, v[4:7] offset:1024
	ds_write_b128 v209, v[8:11] offset:2048
	ds_write_b128 v209, v[12:15] offset:3072
	ds_write_b128 v209, v[16:19] offset:16384
	ds_write_b128 v209, v[20:23] offset:17408
	ds_write_b128 v209, v[24:27] offset:18432
	ds_write_b128 v209, v[28:31] offset:19456
	ds_write_b128 v209, v[32:35] offset:32768
	ds_write_b128 v209, v[36:39] offset:33792
	ds_write_b128 v209, v[40:43] offset:34816
	ds_write_b128 v209, v[44:47] offset:35840
	global_load_dwordx4 v[0:3], v132, s[8:9]
	global_load_dwordx4 v[4:7], v132, s[8:9] offset:1024
	global_load_dwordx4 v[8:11], v132, s[8:9] offset:2048
	global_load_dwordx4 v[12:15], v132, s[8:9] offset:3072
	global_load_dwordx4 v[16:19], v132, s[10:11]
	global_load_dwordx4 v[20:23], v132, s[10:11] offset:1024
	global_load_dwordx4 v[24:27], v132, s[10:11] offset:2048
	global_load_dwordx4 v[28:31], v132, s[10:11] offset:3072
	global_load_dwordx4 v[32:35], v133, s[12:13]
	global_load_dwordx4 v[36:39], v133, s[12:13] offset:16
	global_load_dwordx4 v[40:43], v134, s[12:13]
	global_load_dwordx4 v[44:47], v134, s[12:13] offset:16
	s_add_u32 s15, s15, 1
	s_cmp_lt_u32 s15, 0x80
	s_cselect_b32 s14, 0x4000, 0
	s_add_u32 s8, s8, s14
	s_addc_u32 s9, s9, 0
	s_add_u32 s10, s10, s14
	s_addc_u32 s11, s11, 0
	s_add_u32 s12, s12, s14
	s_addc_u32 s13, s13, 0
	s_xor_b32 s3, s3, 0xc000
	s_waitcnt lgkmcnt(0)
	s_barrier
	s_waitcnt vmcnt(36)
	v_add_u32_e32 v209, s3, v208
	ds_write_b128 v209, v[48:51]
	ds_write_b128 v209, v[52:55] offset:1024
	ds_write_b128 v209, v[56:59] offset:2048
	ds_write_b128 v209, v[60:63] offset:3072
	ds_write_b128 v209, v[64:67] offset:16384
	ds_write_b128 v209, v[68:71] offset:17408
	ds_write_b128 v209, v[72:75] offset:18432
	ds_write_b128 v209, v[76:79] offset:19456
	ds_write_b128 v209, v[80:83] offset:32768
	ds_write_b128 v209, v[84:87] offset:33792
	ds_write_b128 v209, v[88:91] offset:34816
	ds_write_b128 v209, v[92:95] offset:35840
	global_load_dwordx4 v[48:51], v132, s[8:9]
	global_load_dwordx4 v[52:55], v132, s[8:9] offset:1024
	global_load_dwordx4 v[56:59], v132, s[8:9] offset:2048
	global_load_dwordx4 v[60:63], v132, s[8:9] offset:3072
	global_load_dwordx4 v[64:67], v132, s[10:11]
	global_load_dwordx4 v[68:71], v132, s[10:11] offset:1024
	global_load_dwordx4 v[72:75], v132, s[10:11] offset:2048
	global_load_dwordx4 v[76:79], v132, s[10:11] offset:3072
	global_load_dwordx4 v[80:83], v133, s[12:13]
	global_load_dwordx4 v[84:87], v133, s[12:13] offset:16
	global_load_dwordx4 v[88:91], v134, s[12:13]
	global_load_dwordx4 v[92:95], v134, s[12:13] offset:16
	s_add_u32 s15, s15, 1
	s_cmp_lt_u32 s15, 0x80
	s_cselect_b32 s14, 0x4000, 0
	s_add_u32 s8, s8, s14
	s_addc_u32 s9, s9, 0
	s_add_u32 s10, s10, s14
	s_addc_u32 s11, s11, 0
	s_add_u32 s12, s12, s14
	s_addc_u32 s13, s13, 0
	s_xor_b32 s3, s3, 0xc000
	s_waitcnt lgkmcnt(0)
	s_barrier
	s_waitcnt vmcnt(36)
	v_add_u32_e32 v209, s3, v208
	ds_write_b128 v209, v[96:99]
	ds_write_b128 v209, v[100:103] offset:1024
	ds_write_b128 v209, v[104:107] offset:2048
	ds_write_b128 v209, v[108:111] offset:3072
	ds_write_b128 v209, v[112:115] offset:16384
	ds_write_b128 v209, v[116:119] offset:17408
	ds_write_b128 v209, v[120:123] offset:18432
	ds_write_b128 v209, v[124:127] offset:19456
	ds_write_b128 v209, v[128:131] offset:32768
	ds_write_b128 v209, v[136:139] offset:33792
	ds_write_b128 v209, v[140:143] offset:34816
	ds_write_b128 v209, v[148:151] offset:35840
	global_load_dwordx4 v[96:99], v132, s[8:9]
	global_load_dwordx4 v[100:103], v132, s[8:9] offset:1024
	global_load_dwordx4 v[104:107], v132, s[8:9] offset:2048
	global_load_dwordx4 v[108:111], v132, s[8:9] offset:3072
	global_load_dwordx4 v[112:115], v132, s[10:11]
	global_load_dwordx4 v[116:119], v132, s[10:11] offset:1024
	global_load_dwordx4 v[120:123], v132, s[10:11] offset:2048
	global_load_dwordx4 v[124:127], v132, s[10:11] offset:3072
	global_load_dwordx4 v[128:131], v133, s[12:13]
	global_load_dwordx4 v[136:139], v133, s[12:13] offset:16
	global_load_dwordx4 v[140:143], v134, s[12:13]
	global_load_dwordx4 v[148:151], v134, s[12:13] offset:16
	s_add_u32 s15, s15, 1
	s_cmp_lt_u32 s15, 0x80
	s_cselect_b32 s14, 0x4000, 0
	s_add_u32 s8, s8, s14
	s_addc_u32 s9, s9, 0
	s_add_u32 s10, s10, s14
	s_addc_u32 s11, s11, 0
	s_add_u32 s12, s12, s14
	s_addc_u32 s13, s13, 0
	s_xor_b32 s3, s3, 0xc000
	s_waitcnt lgkmcnt(0)
	s_barrier
	s_waitcnt vmcnt(36)
	v_add_u32_e32 v209, s3, v208
	ds_write_b128 v209, v[152:155]
	ds_write_b128 v209, v[156:159] offset:1024
	ds_write_b128 v209, v[160:163] offset:2048
	ds_write_b128 v209, v[164:167] offset:3072
	ds_write_b128 v209, v[168:171] offset:16384
	ds_write_b128 v209, v[172:175] offset:17408
	ds_write_b128 v209, v[178:181] offset:18432
	ds_write_b128 v209, v[182:185] offset:19456
	ds_write_b128 v209, v[190:193] offset:32768
	ds_write_b128 v209, v[194:197] offset:33792
	ds_write_b128 v209, v[198:201] offset:34816
	ds_write_b128 v209, v[202:205] offset:35840
	global_load_dwordx4 v[152:155], v132, s[8:9]
	global_load_dwordx4 v[156:159], v132, s[8:9] offset:1024
	global_load_dwordx4 v[160:163], v132, s[8:9] offset:2048
	global_load_dwordx4 v[164:167], v132, s[8:9] offset:3072
	global_load_dwordx4 v[168:171], v132, s[10:11]
	global_load_dwordx4 v[172:175], v132, s[10:11] offset:1024
	global_load_dwordx4 v[178:181], v132, s[10:11] offset:2048
	global_load_dwordx4 v[182:185], v132, s[10:11] offset:3072
	global_load_dwordx4 v[190:193], v133, s[12:13]
	global_load_dwordx4 v[194:197], v133, s[12:13] offset:16
	global_load_dwordx4 v[198:201], v134, s[12:13]
	global_load_dwordx4 v[202:205], v134, s[12:13] offset:16
	s_add_u32 s15, s15, 1
	s_cmp_lt_u32 s15, 0x80
	s_cselect_b32 s14, 0x4000, 0
	s_add_u32 s8, s8, s14
	s_addc_u32 s9, s9, 0
	s_add_u32 s10, s10, s14
	s_addc_u32 s11, s11, 0
	s_add_u32 s12, s12, s14
	s_addc_u32 s13, s13, 0
	s_xor_b32 s3, s3, 0xc000
	s_waitcnt lgkmcnt(0)
	s_barrier
	s_add_u32 s2, s2, 1
	s_cmp_lt_u32 s2, 32
	s_cbranch_scc1 .Lshadow_loop
	s_waitcnt vmcnt(0)
	s_barrier

; DI float bflo(unsigned u) { return __uint_as_float(u << 16); }
; DI float bfhi(unsigned u) { return __uint_as_float(u & 0xffff0000u); }
; DI bf16x8 packS(const f32x16& x, int s) { return pack8(x[8 * s], x[8 * s + 1], x[8 * s + 2], x[8 * s + 3], x[8 * s + 4], x[8 * s + 5], x[8 * s + 6], x[8 * s + 7]); }
; #define SCAN_RDW(F, mh) do { _Pragma("unroll") for (int k = 0; k < 8; ++k) { const int i2 = k >> 2, m = 2 * (mh) + ((k >> 1) & 1), sx = k & 1; F[k] = *(const bf16x8*)(lw + ((i2 * 4 + m) * 2 + sx) * 1024); } } while (0)
; #define SCAN_RDK(F, mh) do { _Pragma("unroll") for (int k = 0; k < 8; ++k) { const int m = 2 * (mh) + (k >> 2), j2 = (k >> 1) & 1, sx = k & 1; F[k] = *(const bf16x8*)(lk + ((m * 2 + j2) * 2 + sx) * 1024); } } while (0)
; #define SCAN_MMW(F, mh) do { _Pragma("unroll") for (int q = 0; q < 4; ++q) { const int m = 2 * (mh) + (q >> 1), sx = q & 1; vn[0] = MFMA32(F[q], Sb[m][sx], vn[0]); vn[1] = MFMA32(F[4 + q], Sb[m][sx], vn[1]); } } while (0)
; DI void gdn_scan_seq(const Params& p, int bh16, char* ldsf) {
;     ...
;     char* sco = scp + (size_t)c * 32768;
;     bf16x8 Sb[4][2];
; #pragma unroll
;     for (int m = 0; m < 4; ++m) { Sb[m][0] = packS(S[m], 0); Sb[m][1] = packS(S[m], 1); *(bf16x8*)(sco + (m * 2 + 0) * 1024) = Sb[m][0]; *(bf16x8*)(sco + (m * 2 + 1) * 1024) = Sb[m][1]; }
;     __builtin_amdgcn_sched_barrier(0);
;     if (c + 2 < 128) { const int s2 = sl >= 1 ? sl - 1 : 2; SCAN_ISSUE(c + 2, s2); }
;     const char* base = ldsf + sl * 49152;
;     const char* lw = base + lane * 16; const char* lk = lw + 16384; const char* lu = base + 32768 + wv * 4096 + lane * 16;
;     const float gl = glt[c];
;     f32x16 vn[2];
; #pragma unroll
;     for (int i2 = 0; i2 < 2; ++i2) {
;       const u32x4 ua = *(const u32x4*)(lu + (2 * i2) * 1024), ub = *(const u32x4*)(lu + (2 * i2 + 1) * 1024);
; #pragma unroll
;       for (int e = 0; e < 4; ++e) { vn[i2][2 * e] = bflo(ua[e]); vn[i2][2 * e + 1] = bfhi(ua[e]); vn[i2][8 + 2 * e] = bflo(ub[e]); vn[i2][8 + 2 * e + 1] = bfhi(ub[e]); }
;     }
;     bf16x8 fa[8], fb[8];
;     ...
;     SCAN_RDW(fa, 0);
;     __builtin_amdgcn_sched_barrier(0);
;     SCAN_RDW(fb, 1);
;     __builtin_amdgcn_sched_barrier(0);
;     SCAN_MMW(fa, 0);
;     __builtin_amdgcn_sched_barrier(0);
;     SCAN_RDK(fa, 0);
.Lscan_loop:
	s_barrier
	v_add_u32_e32 v131, s3, v130
	v_add_u32_e32 v134, s3, v129
	v_mov_b32_e32 v143, s18
	ds_read_b128 v[72:75], v134 offset:32768
	ds_read_b128 v[76:79], v134 offset:33792
	ds_read_b32 v142, v143
	ds_read_b128 v[148:151], v131 offset:0
	ds_read_b128 v[152:155], v131 offset:1024
	ds_read_b128 v[156:159], v131 offset:2048
	ds_read_b128 v[160:163], v131 offset:3072
	ds_read_b128 v[164:167], v131 offset:4096
	ds_read_b128 v[168:171], v131 offset:5120
	ds_read_b128 v[172:175], v131 offset:6144
	ds_read_b128 v[178:181], v131 offset:7168
	ds_read_b128 v[88:91], v134 offset:34816
	ds_read_b128 v[92:95], v134 offset:35840
	s_waitcnt lgkmcnt(10)
	v_mfma_f32_32x32x16_bf16 v[0:15], v[182:185], v[80:83], v[0:15]
	v_lshlrev_b32_e32 v64, 16, v72
	v_and_b32_e32 v65, 0xffff0000, v72
	v_lshlrev_b32_e32 v66, 16, v73
	v_and_b32_e32 v67, 0xffff0000, v73
	v_lshlrev_b32_e32 v68, 16, v74
	v_mfma_f32_32x32x16_bf16 v[0:15], v[190:193], v[84:87], v[0:15]
	v_and_b32_e32 v69, 0xffff0000, v74
	v_lshlrev_b32_e32 v70, 16, v75
	v_and_b32_e32 v71, 0xffff0000, v75
	v_lshlrev_b32_e32 v72, 16, v76
	v_and_b32_e32 v73, 0xffff0000, v76
	v_mfma_f32_32x32x16_bf16 v[16:31], v[194:197], v[80:83], v[16:31]
	v_lshlrev_b32_e32 v74, 16, v77
	v_and_b32_e32 v75, 0xffff0000, v77
	v_lshlrev_b32_e32 v76, 16, v78
	v_and_b32_e32 v77, 0xffff0000, v78
	v_mfma_f32_32x32x16_bf16 v[16:31], v[198:201], v[84:87], v[16:31]
	v_lshlrev_b32_e32 v78, 16, v79
	v_and_b32_e32 v79, 0xffff0000, v79
	s_nop 1
	v_mfma_f32_32x32x16_bf16 v[32:47], v[202:205], v[80:83], v[32:47]
	v_cvt_pk_bf16_f32 v96, v0, v1
	v_cvt_pk_bf16_f32 v97, v2, v3
	v_cvt_pk_bf16_f32 v98, v4, v5
	v_cvt_pk_bf16_f32 v99, v6, v7
	v_cvt_pk_bf16_f32 v100, v8, v9
	v_mfma_f32_32x32x16_bf16 v[32:47], v[208:211], v[84:87], v[32:47]
	v_cvt_pk_bf16_f32 v101, v10, v11
	v_cvt_pk_bf16_f32 v102, v12, v13
	v_cvt_pk_bf16_f32 v103, v14, v15
	s_nop 1
	v_mfma_f32_32x32x16_bf16 v[48:63], v[212:215], v[80:83], v[48:63]
	v_cvt_pk_bf16_f32 v104, v16, v17
	v_cvt_pk_bf16_f32 v105, v18, v19
	v_cvt_pk_bf16_f32 v106, v20, v21
	v_cvt_pk_bf16_f32 v107, v22, v23
	v_cvt_pk_bf16_f32 v108, v24, v25
	v_mfma_f32_32x32x16_bf16 v[48:63], v[216:219], v[84:87], v[48:63]
	v_cvt_pk_bf16_f32 v109, v26, v27
	v_cvt_pk_bf16_f32 v110, v28, v29
	v_cvt_pk_bf16_f32 v111, v30, v31
	s_waitcnt lgkmcnt(0)
	ds_read_b128 v[182:185], v131 offset:8192
	ds_read_b128 v[190:193], v131 offset:9216
	ds_read_b128 v[194:197], v131 offset:10240
	ds_read_b128 v[198:201], v131 offset:11264
	ds_read_b128 v[202:205], v131 offset:12288
	ds_read_b128 v[208:211], v131 offset:13312
	ds_read_b128 v[212:215], v131 offset:14336
	ds_read_b128 v[216:219], v131 offset:15360
	v_mfma_f32_32x32x16_bf16 v[64:79], v[148:151], v[96:99], v[64:79]
	v_cvt_pk_bf16_f32 v112, v32, v33
	v_cvt_pk_bf16_f32 v113, v34, v35
	v_cvt_pk_bf16_f32 v114, v36, v37
	v_cvt_pk_bf16_f32 v115, v38, v39
	v_cvt_pk_bf16_f32 v116, v40, v41
	v_mfma_f32_32x32x16_bf16 v[64:79], v[152:155], v[100:103], v[64:79]
	v_cvt_pk_bf16_f32 v117, v42, v43
	v_cvt_pk_bf16_f32 v118, v44, v45
	v_cvt_pk_bf16_f32 v119, v46, v47
	v_cvt_pk_bf16_f32 v120, v48, v49
	v_cvt_pk_bf16_f32 v121, v50, v51
	v_mfma_f32_32x32x16_bf16 v[64:79], v[156:159], v[104:107], v[64:79]
	v_cvt_pk_bf16_f32 v122, v52, v53
	v_cvt_pk_bf16_f32 v123, v54, v55
	v_cvt_pk_bf16_f32 v124, v56, v57
	v_cvt_pk_bf16_f32 v125, v58, v59
	v_cvt_pk_bf16_f32 v126, v60, v61
	v_mfma_f32_32x32x16_bf16 v[64:79], v[160:163], v[108:111], v[64:79]
	v_cvt_pk_bf16_f32 v127, v62, v63
	v_lshlrev_b32_e32 v80, 16, v88
	v_and_b32_e32 v81, 0xffff0000, v88
	v_lshlrev_b32_e32 v82, 16, v89
	v_and_b32_e32 v83, 0xffff0000, v89
	v_mfma_f32_32x32x16_bf16 v[64:79], v[164:167], v[112:115], v[64:79]
	v_lshlrev_b32_e32 v84, 16, v90
	v_and_b32_e32 v85, 0xffff0000, v90
	v_lshlrev_b32_e32 v86, 16, v91
	v_and_b32_e32 v87, 0xffff0000, v91
	global_store_dwordx4 v128, v[96:99], s[8:9]
	v_mfma_f32_32x32x16_bf16 v[64:79], v[168:171], v[116:119], v[64:79]
	v_lshlrev_b32_e32 v88, 16, v92
	v_and_b32_e32 v89, 0xffff0000, v92
	v_lshlrev_b32_e32 v90, 16, v93
	v_and_b32_e32 v91, 0xffff0000, v93
	global_store_dwordx4 v128, v[100:103], s[8:9] offset:1024
	v_mfma_f32_32x32x16_bf16 v[64:79], v[172:175], v[120:123], v[64:79]
	v_lshlrev_b32_e32 v92, 16, v94
	v_and_b32_e32 v93, 0xffff0000, v94
	v_lshlrev_b32_e32 v94, 16, v95
	v_and_b32_e32 v95, 0xffff0000, v95
	global_store_dwordx4 v128, v[104:107], s[8:9] offset:2048
	v_mfma_f32_32x32x16_bf16 v[64:79], v[178:181], v[124:127], v[64:79]
	v_pk_mul_f32 v[0:1], v[0:1], v[142:143] op_sel_hi:[1,0]
	v_pk_mul_f32 v[2:3], v[2:3], v[142:143] op_sel_hi:[1,0]
	v_pk_mul_f32 v[4:5], v[4:5], v[142:143] op_sel_hi:[1,0]
	v_pk_mul_f32 v[6:7], v[6:7], v[142:143] op_sel_hi:[1,0]
	global_store_dwordx4 v128, v[108:111], s[8:9] offset:3072
	s_waitcnt lgkmcnt(0)
; DI bf16x8 packS(const f32x16& x, int s) { return pack8(x[8 * s], x[8 * s + 1], x[8 * s + 2], x[8 * s + 3], x[8 * s + 4], x[8 * s + 5], x[8 * s + 6], x[8 * s + 7]); }
; #define SCAN_RDK(F, mh) do { _Pragma("unroll") for (int k = 0; k < 8; ++k) { const int m = 2 * (mh) + (k >> 2), j2 = (k >> 1) & 1, sx = k & 1; F[k] = *(const bf16x8*)(lk + ((m * 2 + j2) * 2 + sx) * 1024); } } while (0)
; #define SCAN_MMW(F, mh) do { _Pragma("unroll") for (int q = 0; q < 4; ++q) { const int m = 2 * (mh) + (q >> 1), sx = q & 1; vn[0] = MFMA32(F[q], Sb[m][sx], vn[0]); vn[1] = MFMA32(F[4 + q], Sb[m][sx], vn[1]); } } while (0)
; #define SCAN_MMK(F, mh) do { _Pragma("unroll") for (int q = 0; q < 4; ++q) { const int j2 = q >> 1, sx = q & 1; S[2 * (mh)] = MFMA32(F[q], Vb[j2][sx], S[2 * (mh)]); S[2 * (mh) + 1] = MFMA32(F[4 + q], Vb[j2][sx], S[2 * (mh) + 1]); } } while (0)
; DI void gdn_scan_seq(const Params& p, int bh16, char* ldsf) {
;     ...
;     SCAN_RDK(fa, 0);
;     __builtin_amdgcn_sched_barrier(0);
;     SCAN_MMW(fb, 1);
;     __builtin_amdgcn_sched_barrier(0);
;     SCAN_RDK(fb, 1);
;     __builtin_amdgcn_sched_barrier(0);
;     bf16x8 Vb[2][2];
; #pragma unroll
;     for (int j2 = 0; j2 < 2; ++j2) { Vb[j2][0] = packS(vn[j2], 0); Vb[j2][1] = packS(vn[j2], 1); }
; #pragma unroll
;     for (int m = 0; m < 4; ++m)
; #pragma unroll
;       for (int r = 0; r < 16; ++r) S[m][r] *= gl;
;     SCAN_MMK(fa, 0);
;     SCAN_MMK(fb, 1);
;     ...
;     asm volatile("s_waitcnt lgkmcnt(0)" ::: "memory");
;     sl = sl == 2 ? 0 : sl + 1;
;   }
	ds_read_b128 v[148:151], v131 offset:16384
	ds_read_b128 v[152:155], v131 offset:17408
	ds_read_b128 v[156:159], v131 offset:20480
	ds_read_b128 v[160:163], v131 offset:21504
	ds_read_b128 v[164:167], v131 offset:24576
	ds_read_b128 v[168:171], v131 offset:25600
	ds_read_b128 v[172:175], v131 offset:28672
	ds_read_b128 v[178:181], v131 offset:29696
	v_mfma_f32_32x32x16_bf16 v[80:95], v[182:185], v[96:99], v[80:95]
	v_pk_mul_f32 v[8:9], v[8:9], v[142:143] op_sel_hi:[1,0]
	v_pk_mul_f32 v[10:11], v[10:11], v[142:143] op_sel_hi:[1,0]
	v_pk_mul_f32 v[12:13], v[12:13], v[142:143] op_sel_hi:[1,0]
	v_pk_mul_f32 v[14:15], v[14:15], v[142:143] op_sel_hi:[1,0]
	global_store_dwordx4 v128, v[112:115], s[10:11]
	v_mfma_f32_32x32x16_bf16 v[80:95], v[190:193], v[100:103], v[80:95]
	v_pk_mul_f32 v[16:17], v[16:17], v[142:143] op_sel_hi:[1,0]
	v_pk_mul_f32 v[18:19], v[18:19], v[142:143] op_sel_hi:[1,0]
	v_pk_mul_f32 v[20:21], v[20:21], v[142:143] op_sel_hi:[1,0]
	v_pk_mul_f32 v[22:23], v[22:23], v[142:143] op_sel_hi:[1,0]
	global_store_dwordx4 v128, v[116:119], s[10:11] offset:1024
	v_mfma_f32_32x32x16_bf16 v[80:95], v[194:197], v[104:107], v[80:95]
	v_pk_mul_f32 v[24:25], v[24:25], v[142:143] op_sel_hi:[1,0]
	v_pk_mul_f32 v[26:27], v[26:27], v[142:143] op_sel_hi:[1,0]
	v_pk_mul_f32 v[28:29], v[28:29], v[142:143] op_sel_hi:[1,0]
	v_pk_mul_f32 v[30:31], v[30:31], v[142:143] op_sel_hi:[1,0]
	global_store_dwordx4 v128, v[120:123], s[10:11] offset:2048
	v_mfma_f32_32x32x16_bf16 v[80:95], v[198:201], v[108:111], v[80:95]
	v_pk_mul_f32 v[32:33], v[32:33], v[142:143] op_sel_hi:[1,0]
	v_pk_mul_f32 v[34:35], v[34:35], v[142:143] op_sel_hi:[1,0]
	v_pk_mul_f32 v[36:37], v[36:37], v[142:143] op_sel_hi:[1,0]
	v_pk_mul_f32 v[38:39], v[38:39], v[142:143] op_sel_hi:[1,0]
	global_store_dwordx4 v128, v[124:127], s[10:11] offset:3072
	v_mfma_f32_32x32x16_bf16 v[80:95], v[202:205], v[112:115], v[80:95]
	v_pk_mul_f32 v[40:41], v[40:41], v[142:143] op_sel_hi:[1,0]
	v_pk_mul_f32 v[42:43], v[42:43], v[142:143] op_sel_hi:[1,0]
	v_pk_mul_f32 v[44:45], v[44:45], v[142:143] op_sel_hi:[1,0]
	v_pk_mul_f32 v[46:47], v[46:47], v[142:143] op_sel_hi:[1,0]
	v_mfma_f32_32x32x16_bf16 v[80:95], v[208:211], v[116:119], v[80:95]
	v_pk_mul_f32 v[48:49], v[48:49], v[142:143] op_sel_hi:[1,0]
	v_pk_mul_f32 v[50:51], v[50:51], v[142:143] op_sel_hi:[1,0]
	v_pk_mul_f32 v[52:53], v[52:53], v[142:143] op_sel_hi:[1,0]
	v_pk_mul_f32 v[54:55], v[54:55], v[142:143] op_sel_hi:[1,0]
	v_cvt_pk_bf16_f32 v64, v64, v65
	v_mfma_f32_32x32x16_bf16 v[80:95], v[212:215], v[120:123], v[80:95]
	v_pk_mul_f32 v[56:57], v[56:57], v[142:143] op_sel_hi:[1,0]
	v_pk_mul_f32 v[58:59], v[58:59], v[142:143] op_sel_hi:[1,0]
	v_pk_mul_f32 v[60:61], v[60:61], v[142:143] op_sel_hi:[1,0]
	v_pk_mul_f32 v[62:63], v[62:63], v[142:143] op_sel_hi:[1,0]
	v_cvt_pk_bf16_f32 v65, v66, v67
	v_mfma_f32_32x32x16_bf16 v[80:95], v[216:219], v[124:127], v[80:95]
	v_cvt_pk_bf16_f32 v66, v68, v69
	v_cvt_pk_bf16_f32 v67, v70, v71
	v_cvt_pk_bf16_f32 v68, v72, v73
	v_cvt_pk_bf16_f32 v69, v74, v75
	v_cvt_pk_bf16_f32 v70, v76, v77
	v_cvt_pk_bf16_f32 v71, v78, v79
	s_waitcnt lgkmcnt(0)
	ds_read_b128 v[182:185], v131 offset:18432
	ds_read_b128 v[190:193], v131 offset:19456
	ds_read_b128 v[194:197], v131 offset:22528
	ds_read_b128 v[198:201], v131 offset:23552
	ds_read_b128 v[202:205], v131 offset:26624
	ds_read_b128 v[208:211], v131 offset:27648
	ds_read_b128 v[212:215], v131 offset:30720
	ds_read_b128 v[216:219], v131 offset:31744
	v_mfma_f32_32x32x16_bf16 v[0:15], v[148:151], v[64:67], v[0:15]
	s_add_u32 s2, s2, 1
	s_xor_b32 s3, s3, 0xc000
	s_add_u32 s18, s18, 4
	v_mfma_f32_32x32x16_bf16 v[0:15], v[152:155], v[68:71], v[0:15]
	s_add_u32 s8, s8, 0x8000
	s_addc_u32 s9, s9, 0
	s_add_u32 s10, s10, 0x8000
	s_addc_u32 s11, s11, 0
	v_mfma_f32_32x32x16_bf16 v[16:31], v[156:159], v[64:67], v[16:31]
	s_nop 0
	s_nop 0
	v_mfma_f32_32x32x16_bf16 v[16:31], v[160:163], v[68:71], v[16:31]
	v_cvt_pk_bf16_f32 v80, v80, v81
	v_cvt_pk_bf16_f32 v81, v82, v83
	v_mfma_f32_32x32x16_bf16 v[32:47], v[164:167], v[64:67], v[32:47]
	v_cvt_pk_bf16_f32 v82, v84, v85
	v_cvt_pk_bf16_f32 v83, v86, v87
	v_mfma_f32_32x32x16_bf16 v[32:47], v[168:171], v[68:71], v[32:47]
	v_cvt_pk_bf16_f32 v84, v88, v89
	v_cvt_pk_bf16_f32 v85, v90, v91
	v_mfma_f32_32x32x16_bf16 v[48:63], v[172:175], v[64:67], v[48:63]
	v_cvt_pk_bf16_f32 v86, v92, v93
	v_cvt_pk_bf16_f32 v87, v94, v95
	v_mfma_f32_32x32x16_bf16 v[48:63], v[178:181], v[68:71], v[48:63]
	s_cmp_lt_u32 s2, 0x80
	s_waitcnt lgkmcnt(0)
	s_cbranch_scc1 .Lscan_loop
	s_waitcnt vmcnt(0)
	s_barrier
